# baseline (speedup 1.0000x reference)
_Z16sum_layer_kernelPKfS0_Pf:
	s_load_dwordx4 s[4:7], s[0:1], 0x0
	s_load_dwordx2 s[8:9], s[0:1], 0x10
	v_lshrrev_b32_e32 v42, 6, v0
	v_bfe_u32 v41, v0, 5, 1
	v_and_b32_e32 v40, 31, v0
	v_readfirstlane_b32 s23, v42
	v_and_b32_e32 v43, 7, v0
	v_bfe_u32 v44, v0, 3, 3
	s_lshl_b32 s3, s2, 12
	s_lshl_b32 s19, s2, 7
	s_lshl_b32 s23, s23, 12
	v_lshlrev_b32_e32 v1, 11, v41
	v_lshl_or_b32 v1, v40, 2, v1
	s_mov_b32 m0, s23
	v_lshrrev_b32_e32 v46, 1, v44
	v_xor_b32_e32 v46, v43, v46
	v_lshlrev_b32_e32 v46, 4, v46
	v_lshl_add_u32 v35, v44, 16, v46
	v_lshl_add_u32 v35, v42, 21, v35
	v_add_u32_e32 v35, s19, v35
	v_xor_b32_e32 v86, 64, v35
	s_mov_b32 s20, 0x7fc00
	s_mov_b32 s21, 0xff800
	s_mov_b32 s22, 0x17f400
	s_mov_b32 s14, 0x200000
	s_mov_b32 s15, 0x20000
	s_waitcnt lgkmcnt(0)
	s_mov_b32 s12, s6
	s_and_b32 s13, s7, 0xffff
	s_and_b32 s5, s5, 0xffff
	s_mov_b32 s6, 0x800000
	s_mov_b32 s7, s15
	buffer_load_dword v18, v1, s[12:15], s3 offen nt
	buffer_load_dword v19, v1, s[12:15], s3 offen offset:128 nt
	buffer_load_dword v20, v1, s[12:15], s3 offen offset:256 nt
	buffer_load_dword v21, v1, s[12:15], s3 offen offset:384 nt
	buffer_load_dword v22, v1, s[12:15], s3 offen offset:512 nt
	buffer_load_dword v23, v1, s[12:15], s3 offen offset:640 nt
	buffer_load_dword v24, v1, s[12:15], s3 offen offset:768 nt
	buffer_load_dword v25, v1, s[12:15], s3 offen offset:896 nt
	buffer_load_dword v26, v1, s[12:15], s3 offen offset:1024 nt
	buffer_load_dword v27, v1, s[12:15], s3 offen offset:1152 nt
	buffer_load_dword v28, v1, s[12:15], s3 offen offset:1280 nt
	buffer_load_dword v29, v1, s[12:15], s3 offen offset:1408 nt
	buffer_load_dword v30, v1, s[12:15], s3 offen offset:1536 nt
	buffer_load_dword v31, v1, s[12:15], s3 offen offset:1664 nt
	buffer_load_dword v32, v1, s[12:15], s3 offen offset:1792 nt
	buffer_load_dword v33, v1, s[12:15], s3 offen offset:1920 nt
	buffer_load_dwordx4 v35, s[4:7], 0 offen nt lds
	buffer_load_dwordx4 v86, s[4:7], s20 offen offset:1024 nt lds
	buffer_load_dwordx4 v35, s[4:7], s21 offen offset:2048 nt lds
	buffer_load_dwordx4 v86, s[4:7], s22 offen offset:3072 nt lds
	v_and_b32_e32 v45, 63, v0
	v_lshlrev_b32_e32 v36, 2, v40
	v_lshl_add_u32 v36, v41, 18, v36
	v_lshl_add_u32 v36, v42, 21, v36
	v_add_u32_e32 v36, s19, v36
	v_bfe_u32 v47, v40, 1, 3
	v_lshlrev_b32_e32 v39, 2, v41
	v_xor_b32_e32 v39, v39, v47
	v_lshlrev_b32_e32 v39, 4, v39
	v_lshl_add_u32 v39, v40, 7, v39
	v_lshl_add_u32 v39, v42, 12, v39
	v_xor_b32_e32 v81, 16, v39
	v_xor_b32_e32 v82, 32, v39
	v_xor_b32_e32 v83, 48, v39
	v_cmp_gt_u32_e32 vcc, 32, v45
	v_mov_b32_e32 v34, 0xc1600000
	v_mov_b32_e32 v84, 0x3fb8aa3b
	v_mov_b32_e32 v85, 0x3f317218
	s_lshl_b32 s24, 1, 16
	s_lshl_b32 s25, 2, 16
	s_lshl_b32 s26, 3, 16
	s_lshl_b32 s27, 8, 16
	s_lshl_b32 s28, 9, 16
	s_lshl_b32 s29, 10, 16
	s_lshl_b32 s30, 11, 16
	s_lshl_b32 s31, 16, 16
	s_lshl_b32 s32, 17, 16
	s_lshl_b32 s33, 18, 16
	s_lshl_b32 s34, 19, 16
	s_lshl_b32 s35, 24, 16
	s_lshl_b32 s36, 25, 16
	s_lshl_b32 s37, 26, 16
	s_lshl_b32 s38, 27, 16
	s_and_b32 s9, s9, 0xffff
	s_mov_b32 s10, s6
	s_mov_b32 s11, s15
	s_waitcnt vmcnt(4)
	v_max3_f32 v48, v18, v19, v20
	v_max3_f32 v50, v21, v22, v23
	v_max3_f32 v48, v48, v24, v25
	v_max3_f32 v50, v50, v26, v27
	v_max3_f32 v48, v48, v28, v29
	v_max3_f32 v50, v50, v30, v31
	v_max3_f32 v48, v48, v32, v33
	v_max_f32_e32 v48, v48, v50
	v_mov_b32_e32 v50, v48
	s_nop 1
	v_permlane32_swap_b32_e32 v48, v50
	v_max_f32_e32 v48, v48, v50
	v_fmamk_f32 v48, v48, 0x3fb8aa3b, v34
	v_pk_fma_f32 v[18:19], v[18:19], v[84:85], v[48:49] op_sel_hi:[1,0,0] neg_lo:[0,0,1] neg_hi:[0,0,1]
	v_exp_f32_e32 v18, v18
	v_exp_f32_e32 v19, v19
	v_pk_fma_f32 v[20:21], v[20:21], v[84:85], v[48:49] op_sel_hi:[1,0,0] neg_lo:[0,0,1] neg_hi:[0,0,1]
	v_exp_f32_e32 v20, v20
	v_exp_f32_e32 v21, v21
	v_pk_fma_f32 v[22:23], v[22:23], v[84:85], v[48:49] op_sel_hi:[1,0,0] neg_lo:[0,0,1] neg_hi:[0,0,1]
	v_exp_f32_e32 v22, v22
	v_exp_f32_e32 v23, v23
	v_pk_fma_f32 v[24:25], v[24:25], v[84:85], v[48:49] op_sel_hi:[1,0,0] neg_lo:[0,0,1] neg_hi:[0,0,1]
	v_exp_f32_e32 v24, v24
	v_exp_f32_e32 v25, v25
	v_pk_fma_f32 v[26:27], v[26:27], v[84:85], v[48:49] op_sel_hi:[1,0,0] neg_lo:[0,0,1] neg_hi:[0,0,1]
	v_exp_f32_e32 v26, v26
	v_exp_f32_e32 v27, v27
	v_pk_fma_f32 v[28:29], v[28:29], v[84:85], v[48:49] op_sel_hi:[1,0,0] neg_lo:[0,0,1] neg_hi:[0,0,1]
	v_exp_f32_e32 v28, v28
	v_exp_f32_e32 v29, v29
	v_pk_fma_f32 v[30:31], v[30:31], v[84:85], v[48:49] op_sel_hi:[1,0,0] neg_lo:[0,0,1] neg_hi:[0,0,1]
	v_exp_f32_e32 v30, v30
	v_exp_f32_e32 v31, v31
	v_pk_fma_f32 v[32:33], v[32:33], v[84:85], v[48:49] op_sel_hi:[1,0,0] neg_lo:[0,0,1] neg_hi:[0,0,1]
	v_exp_f32_e32 v32, v32
	v_exp_f32_e32 v33, v33
	v_pk_add_f32 v[56:57], v[18:19], v[20:21]
	v_pk_add_f32 v[58:59], v[22:23], v[24:25]
	v_pk_add_f32 v[60:61], v[26:27], v[28:29]
	v_pk_add_f32 v[62:63], v[30:31], v[32:33]
	v_pk_add_f32 v[56:57], v[56:57], v[58:59]
	v_pk_add_f32 v[60:61], v[60:61], v[62:63]
	v_pk_add_f32 v[56:57], v[56:57], v[60:61]
	v_add_f32_e32 v50, v56, v57
	v_mov_b32_e32 v51, v50
	s_nop 1
	v_permlane32_swap_b32_e32 v50, v51
	v_add_f32_e32 v50, v50, v51
	v_log_f32_e32 v50, v50
	v_cvt_pk_f16_f32 v40, v18, v19
	v_cvt_pk_f16_f32 v41, v20, v21
	v_cvt_pk_f16_f32 v42, v22, v23
	v_cvt_pk_f16_f32 v43, v24, v25
	v_cvt_pk_f16_f32 v44, v26, v27
	v_cvt_pk_f16_f32 v45, v28, v29
	v_cvt_pk_f16_f32 v46, v30, v31
	v_cvt_pk_f16_f32 v47, v32, v33
	v_add_f32_e32 v50, 0x41600000, v50
	v_mul_f32_e32 v50, 0xbf317218, v50
	v_cndmask_b32_e64 v51, v50, 1.0, vcc
	s_waitcnt vmcnt(0)
	ds_read_b128 v[2:5], v39
	ds_read_b128 v[6:9], v81
	ds_read_b128 v[10:13], v82
	ds_read_b128 v[14:17], v83
	s_waitcnt lgkmcnt(2)
	v_max3_f32 v52, v2, v3, v4
	v_max3_f32 v53, v5, v6, v7
	v_max_f32_e32 v52, v52, v8
	v_max_f32_e32 v53, v53, v9
	s_waitcnt lgkmcnt(0)
	v_max3_f32 v52, v52, v10, v11
	v_max3_f32 v53, v53, v12, v13
	v_max3_f32 v52, v52, v14, v15
	v_max3_f32 v53, v53, v16, v17
	v_max_f32_e32 v52, v52, v53
	v_mov_b32_e32 v53, v52
	s_nop 1
	v_permlane32_swap_b32_e32 v52, v53
	v_max_f32_e32 v52, v52, v53
	v_cndmask_b32_e32 v54, 1.0, v52, vcc
	v_fmamk_f32 v48, v52, 0x3fb8aa3b, v34
	v_pk_fma_f32 v[2:3], v[2:3], v[84:85], v[48:49] op_sel_hi:[1,0,0] neg_lo:[0,0,1] neg_hi:[0,0,1]
	v_mfma_f32_32x32x2_f32 v[64:79], v54, v51, 0
	v_exp_f32_e32 v2, v2
	v_exp_f32_e32 v3, v3
	v_pk_fma_f32 v[4:5], v[4:5], v[84:85], v[48:49] op_sel_hi:[1,0,0] neg_lo:[0,0,1] neg_hi:[0,0,1]
	v_exp_f32_e32 v4, v4
	v_exp_f32_e32 v5, v5
	v_pk_fma_f32 v[6:7], v[6:7], v[84:85], v[48:49] op_sel_hi:[1,0,0] neg_lo:[0,0,1] neg_hi:[0,0,1]
	v_exp_f32_e32 v6, v6
	v_exp_f32_e32 v7, v7
	v_pk_fma_f32 v[8:9], v[8:9], v[84:85], v[48:49] op_sel_hi:[1,0,0] neg_lo:[0,0,1] neg_hi:[0,0,1]
	v_exp_f32_e32 v8, v8
	v_exp_f32_e32 v9, v9
	v_pk_fma_f32 v[10:11], v[10:11], v[84:85], v[48:49] op_sel_hi:[1,0,0] neg_lo:[0,0,1] neg_hi:[0,0,1]
	v_exp_f32_e32 v10, v10
	v_cvt_pk_f16_f32 v56, v2, v3
	v_cvt_pk_f16_f32 v57, v4, v5
	v_cvt_pk_f16_f32 v58, v6, v7
	v_cvt_pk_f16_f32 v59, v8, v9
	v_exp_f32_e32 v11, v11
	v_pk_fma_f32 v[12:13], v[12:13], v[84:85], v[48:49] op_sel_hi:[1,0,0] neg_lo:[0,0,1] neg_hi:[0,0,1]
	v_exp_f32_e32 v12, v12
	v_mfma_f32_32x32x16_f16 v[18:33], v[56:59], v[40:43], 0
	v_exp_f32_e32 v13, v13
	v_pk_fma_f32 v[14:15], v[14:15], v[84:85], v[48:49] op_sel_hi:[1,0,0] neg_lo:[0,0,1] neg_hi:[0,0,1]
	v_exp_f32_e32 v14, v14
	v_exp_f32_e32 v15, v15
	v_pk_fma_f32 v[16:17], v[16:17], v[84:85], v[48:49] op_sel_hi:[1,0,0] neg_lo:[0,0,1] neg_hi:[0,0,1]
	v_exp_f32_e32 v16, v16
	v_exp_f32_e32 v17, v17
	v_cvt_pk_f16_f32 v60, v10, v11
	v_cvt_pk_f16_f32 v61, v12, v13
	v_cvt_pk_f16_f32 v62, v14, v15
	v_cvt_pk_f16_f32 v63, v16, v17
	s_nop 1
	v_mfma_f32_32x32x16_f16 v[18:33], v[60:63], v[44:47], v[18:33]
	s_nop 11
	v_log_f32_e32 v18, v18
	v_log_f32_e32 v19, v19
	v_log_f32_e32 v20, v20
	v_log_f32_e32 v21, v21
	v_log_f32_e32 v22, v22
	v_log_f32_e32 v23, v23
	v_pk_fma_f32 v[64:65], v[18:19], v[84:85], v[64:65] op_sel:[0,1,0] op_sel_hi:[1,1,1]
	buffer_store_dword v64, v36, s[8:11], 0 offen
	buffer_store_dword v65, v36, s[8:11], s24 offen
	v_log_f32_e32 v24, v24
	v_log_f32_e32 v25, v25
	v_pk_fma_f32 v[66:67], v[20:21], v[84:85], v[66:67] op_sel:[0,1,0] op_sel_hi:[1,1,1]
	buffer_store_dword v66, v36, s[8:11], s25 offen
	buffer_store_dword v67, v36, s[8:11], s26 offen
	v_log_f32_e32 v26, v26
	v_log_f32_e32 v27, v27
	v_pk_fma_f32 v[68:69], v[22:23], v[84:85], v[68:69] op_sel:[0,1,0] op_sel_hi:[1,1,1]
	buffer_store_dword v68, v36, s[8:11], s27 offen
	buffer_store_dword v69, v36, s[8:11], s28 offen
	v_log_f32_e32 v28, v28
	v_log_f32_e32 v29, v29
	v_pk_fma_f32 v[70:71], v[24:25], v[84:85], v[70:71] op_sel:[0,1,0] op_sel_hi:[1,1,1]
	buffer_store_dword v70, v36, s[8:11], s29 offen
	buffer_store_dword v71, v36, s[8:11], s30 offen
	v_log_f32_e32 v30, v30
	v_log_f32_e32 v31, v31
	v_pk_fma_f32 v[72:73], v[26:27], v[84:85], v[72:73] op_sel:[0,1,0] op_sel_hi:[1,1,1]
	buffer_store_dword v72, v36, s[8:11], s31 offen
	buffer_store_dword v73, v36, s[8:11], s32 offen
	v_log_f32_e32 v32, v32
	v_log_f32_e32 v33, v33
	v_pk_fma_f32 v[74:75], v[28:29], v[84:85], v[74:75] op_sel:[0,1,0] op_sel_hi:[1,1,1]
	buffer_store_dword v74, v36, s[8:11], s33 offen
	buffer_store_dword v75, v36, s[8:11], s34 offen
	v_pk_fma_f32 v[76:77], v[30:31], v[84:85], v[76:77] op_sel:[0,1,0] op_sel_hi:[1,1,1]
	buffer_store_dword v76, v36, s[8:11], s35 offen
	buffer_store_dword v77, v36, s[8:11], s36 offen
	v_pk_fma_f32 v[78:79], v[32:33], v[84:85], v[78:79] op_sel:[0,1,0] op_sel_hi:[1,1,1]
	buffer_store_dword v78, v36, s[8:11], s37 offen
	buffer_store_dword v79, v36, s[8:11], s38 offen
	s_endpgm
